# sel: next-triple descriptor read one triple ahead (no LDS round trip before the barrier), two late V^T reads deferred into the exp phase with counted waits
# baseline (speedup 1.0000x reference)
; #define GAS __attribute__((address_space(1)))
; __device__ __forceinline__ unsigned pk4_fp8(float a, float b, float c, float d) { unsigned w = 0u; w = __builtin_amdgcn_cvt_pk_fp8_f32(a, b, w, false); w = __builtin_amdgcn_cvt_pk_fp8_f32(c, d, w, true); return w; }
; __device__ __forceinline__ void gs8_init(GS8& g, const bf16* qrow32) {
; #pragma unroll
;     for (int i = 0; i < 4; ++i) { const u32x4 w = *(const GAS u32x4*)(qrow32 + 8 * i);
;         g.q8[2 * i] = (int)pk4_fp8(bf_lo(w.x) * 8.f, bf_hi(w.x) * 8.f, bf_lo(w.y) * 8.f, bf_hi(w.y) * 8.f); g.q8[2 * i + 1] = (int)pk4_fp8(bf_lo(w.z) * 8.f, bf_hi(w.z) * 8.f, bf_lo(w.w) * 8.f, bf_hi(w.w) * 8.f); }
; #pragma unroll
;     for (int dt = 0; dt < 8; ++dt) g.o[dt] = (f32x4){0.f, 0.f, 0.f, 0.f};
;     g.m = -1e30f; g.l = 0.f;
; }
.LBB0_1782:
	s_cmp_lt_i32 s36, 1
	s_cbranch_scc1 .LBB0_1701
	s_waitcnt vmcnt(0)
	v_lshlrev_b32_e32 v34, 16, v0
	v_and_b32_e32 v0, 0xffff0000, v0
	v_mul_f32_e32 v34, 0x41000000, v34
	v_mul_f32_e32 v35, 0x41000000, v0
	v_mov_b32_e32 v0, v17
	v_cvt_pk_fp8_f32 v0, v34, v35
	v_lshlrev_b32_e32 v36, 16, v1
	v_and_b32_e32 v1, 0xffff0000, v1
	v_mul_f32_e32 v34, 0x41000000, v36
	v_mul_f32_e32 v1, 0x41000000, v1
	v_cvt_pk_fp8_f32 v0, v34, v1 op_sel:[0,0,1]
	v_lshlrev_b32_e32 v1, 16, v2
	v_mul_f32_e32 v34, 0x41000000, v1
	v_and_b32_e32 v1, 0xffff0000, v2
	v_mul_f32_e32 v2, 0x41000000, v1
	v_mov_b32_e32 v1, v17
	v_cvt_pk_fp8_f32 v1, v34, v2
	v_lshlrev_b32_e32 v35, 16, v3
	v_and_b32_e32 v3, 0xffff0000, v3
	v_mul_f32_e32 v2, 0x41000000, v35
	v_mul_f32_e32 v3, 0x41000000, v3
	v_cvt_pk_fp8_f32 v1, v2, v3 op_sel:[0,0,1]
	v_lshlrev_b32_e32 v2, 16, v30
	v_mul_f32_e32 v3, 0x41000000, v2
	v_and_b32_e32 v2, 0xffff0000, v30
	v_mul_f32_e32 v30, 0x41000000, v2
	v_mov_b32_e32 v2, v17
	v_cvt_pk_fp8_f32 v2, v3, v30
	v_lshlrev_b32_e32 v34, 16, v31
	v_and_b32_e32 v30, 0xffff0000, v31
	v_mul_f32_e32 v3, 0x41000000, v34
	v_mul_f32_e32 v30, 0x41000000, v30
	v_cvt_pk_fp8_f32 v2, v3, v30 op_sel:[0,0,1]
	v_lshlrev_b32_e32 v3, 16, v32
	v_mul_f32_e32 v30, 0x41000000, v3
	v_and_b32_e32 v3, 0xffff0000, v32
	v_mul_f32_e32 v31, 0x41000000, v3
	v_mov_b32_e32 v3, v17
	v_cvt_pk_fp8_f32 v3, v30, v31
	v_lshlrev_b32_e32 v32, 16, v33
	v_and_b32_e32 v31, 0xffff0000, v33
	v_mul_f32_e32 v30, 0x41000000, v32
	v_mul_f32_e32 v31, 0x41000000, v31
	v_cvt_pk_fp8_f32 v3, v30, v31 op_sel:[0,0,1]
	v_lshlrev_b32_e32 v30, 16, v4
	v_and_b32_e32 v4, 0xffff0000, v4
	v_mul_f32_e32 v30, 0x41000000, v30
	v_mul_f32_e32 v31, 0x41000000, v4
	v_mov_b32_e32 v4, v17
	v_cvt_pk_fp8_f32 v4, v30, v31
	v_lshlrev_b32_e32 v32, 16, v5
	v_and_b32_e32 v5, 0xffff0000, v5
	v_mul_f32_e32 v30, 0x41000000, v32
	v_mul_f32_e32 v5, 0x41000000, v5
	v_cvt_pk_fp8_f32 v4, v30, v5 op_sel:[0,0,1]
	v_lshlrev_b32_e32 v5, 16, v6
	v_mul_f32_e32 v30, 0x41000000, v5
	v_and_b32_e32 v5, 0xffff0000, v6
	v_mul_f32_e32 v6, 0x41000000, v5
	v_mov_b32_e32 v5, v17
	v_cvt_pk_fp8_f32 v5, v30, v6
	v_lshlrev_b32_e32 v31, 16, v7
	v_and_b32_e32 v7, 0xffff0000, v7
	v_mul_f32_e32 v6, 0x41000000, v31
	v_mul_f32_e32 v7, 0x41000000, v7
	v_cvt_pk_fp8_f32 v5, v6, v7 op_sel:[0,0,1]
	v_lshlrev_b32_e32 v6, 16, v26
	v_mul_f32_e32 v7, 0x41000000, v6
	v_and_b32_e32 v6, 0xffff0000, v26
	v_mul_f32_e32 v26, 0x41000000, v6
	v_mov_b32_e32 v6, v17
	v_cvt_pk_fp8_f32 v6, v7, v26
	v_lshlrev_b32_e32 v30, 16, v27
	v_and_b32_e32 v26, 0xffff0000, v27
	v_mul_f32_e32 v7, 0x41000000, v30
	v_mul_f32_e32 v26, 0x41000000, v26
	v_cvt_pk_fp8_f32 v6, v7, v26 op_sel:[0,0,1]
	v_lshlrev_b32_e32 v7, 16, v28
	v_mul_f32_e32 v26, 0x41000000, v7
	v_and_b32_e32 v7, 0xffff0000, v28
	v_mul_f32_e32 v27, 0x41000000, v7
	v_mov_b32_e32 v7, v17
	v_cvt_pk_fp8_f32 v7, v26, v27
	v_lshlrev_b32_e32 v28, 16, v29
	v_and_b32_e32 v27, 0xffff0000, v29
	v_mul_f32_e32 v26, 0x41000000, v28
	v_mul_f32_e32 v27, 0x41000000, v27
	v_cvt_pk_fp8_f32 v7, v26, v27 op_sel:[0,0,1]
	v_lshlrev_b32_e32 v26, 16, v8
	v_and_b32_e32 v8, 0xffff0000, v8
	v_mul_f32_e32 v26, 0x41000000, v26
	v_mul_f32_e32 v27, 0x41000000, v8
	v_mov_b32_e32 v8, v17
	v_cvt_pk_fp8_f32 v8, v26, v27
	v_lshlrev_b32_e32 v28, 16, v9
	v_and_b32_e32 v9, 0xffff0000, v9
	v_mul_f32_e32 v26, 0x41000000, v28
	v_mul_f32_e32 v9, 0x41000000, v9
	v_cvt_pk_fp8_f32 v8, v26, v9 op_sel:[0,0,1]
	v_lshlrev_b32_e32 v9, 16, v10
	v_mul_f32_e32 v26, 0x41000000, v9
	v_and_b32_e32 v9, 0xffff0000, v10
	v_mul_f32_e32 v10, 0x41000000, v9
	v_mov_b32_e32 v9, v17
	v_cvt_pk_fp8_f32 v9, v26, v10
	v_lshlrev_b32_e32 v27, 16, v11
	v_and_b32_e32 v11, 0xffff0000, v11
	v_mul_f32_e32 v10, 0x41000000, v27
	v_mul_f32_e32 v11, 0x41000000, v11
	v_cvt_pk_fp8_f32 v9, v10, v11 op_sel:[0,0,1]
	v_lshlrev_b32_e32 v10, 16, v22
	v_mul_f32_e32 v11, 0x41000000, v10
	v_and_b32_e32 v10, 0xffff0000, v22
	v_mul_f32_e32 v22, 0x41000000, v10
	v_mov_b32_e32 v10, v17
	v_cvt_pk_fp8_f32 v10, v11, v22
	v_lshlrev_b32_e32 v26, 16, v23
	v_and_b32_e32 v22, 0xffff0000, v23
	v_mul_f32_e32 v11, 0x41000000, v26
	v_mul_f32_e32 v22, 0x41000000, v22
	v_cvt_pk_fp8_f32 v10, v11, v22 op_sel:[0,0,1]
	v_lshlrev_b32_e32 v11, 16, v24
	v_mul_f32_e32 v22, 0x41000000, v11
	v_and_b32_e32 v11, 0xffff0000, v24
	v_mul_f32_e32 v23, 0x41000000, v11
	v_mov_b32_e32 v11, v17
	v_cvt_pk_fp8_f32 v11, v22, v23
	v_lshlrev_b32_e32 v24, 16, v25
	v_and_b32_e32 v23, 0xffff0000, v25
	v_mul_f32_e32 v22, 0x41000000, v24
	v_mul_f32_e32 v23, 0x41000000, v23
	v_cvt_pk_fp8_f32 v11, v22, v23 op_sel:[0,0,1]
; #define RING_BARRIER() do { asm volatile("s_waitcnt lgkmcnt(0)" ::: "memory"); __builtin_amdgcn_s_barrier(); asm volatile("" ::: "memory"); } while (0)
; template <bool DUMMY> __device__ __forceinline__ void sel_phase(Frame& F) {
;     ...
;         u32x2 dcur = PD[F.wave]; unsigned cj = (unsigned)__builtin_amdgcn_readfirstlane((int)dcur.x), cb = (unsigned)__builtin_amdgcn_readfirstlane((int)dcur.y);
;     ...
;         SEL_DMA3(cj, F.lds);
;         for (int p = 0; p < npair; ++p) {
;             u32x2 dnx = {0xffffffffu, 0u}; if (p + 1 < npair) dnx = PD[(p + 1) * 8 + F.wave];
;             asm volatile("s_waitcnt vmcnt(0)" ::: "memory"); RING_BARRIER();
;             const unsigned nj = (unsigned)__builtin_amdgcn_readfirstlane((int)dnx.x), nb = (unsigned)__builtin_amdgcn_readfirstlane((int)dnx.y);
;             if (p + 1 < npair && !(DUMMY && MK_EXP == 2)) { SEL_DMA3(nj, F.lds + ((p + 1) & 1) * 3 * SLOTS); }
	v_lshlrev_b32_e32 v22, 16, v12
	v_and_b32_e32 v12, 0xffff0000, v12
	v_mul_f32_e32 v22, 0x41000000, v22
	v_mul_f32_e32 v23, 0x41000000, v12
	v_mov_b32_e32 v12, v17
	v_cvt_pk_fp8_f32 v12, v22, v23
	v_lshlrev_b32_e32 v24, 16, v13
	v_and_b32_e32 v13, 0xffff0000, v13
	v_mul_f32_e32 v22, 0x41000000, v24
	v_mul_f32_e32 v13, 0x41000000, v13
	v_cvt_pk_fp8_f32 v12, v22, v13 op_sel:[0,0,1]
	v_lshlrev_b32_e32 v13, 16, v14
	v_mul_f32_e32 v22, 0x41000000, v13
	v_and_b32_e32 v13, 0xffff0000, v14
	v_mul_f32_e32 v14, 0x41000000, v13
	v_mov_b32_e32 v13, v17
	v_cvt_pk_fp8_f32 v13, v22, v14
	v_lshlrev_b32_e32 v23, 16, v15
	v_and_b32_e32 v15, 0xffff0000, v15
	v_mul_f32_e32 v14, 0x41000000, v23
	v_mul_f32_e32 v15, 0x41000000, v15
	v_cvt_pk_fp8_f32 v13, v14, v15 op_sel:[0,0,1]
	v_lshlrev_b32_e32 v14, 16, v18
	v_mul_f32_e32 v15, 0x41000000, v14
	v_and_b32_e32 v14, 0xffff0000, v18
	v_mul_f32_e32 v18, 0x41000000, v14
	v_mov_b32_e32 v14, v17
	v_cvt_pk_fp8_f32 v14, v15, v18
	v_lshlrev_b32_e32 v22, 16, v19
	v_and_b32_e32 v18, 0xffff0000, v19
	v_mul_f32_e32 v15, 0x41000000, v22
	v_mul_f32_e32 v18, 0x41000000, v18
	v_cvt_pk_fp8_f32 v14, v15, v18 op_sel:[0,0,1]
	v_lshlrev_b32_e32 v15, 16, v20
	v_mul_f32_e32 v18, 0x41000000, v15
	v_and_b32_e32 v15, 0xffff0000, v20
	v_mul_f32_e32 v19, 0x41000000, v15
	v_mov_b32_e32 v15, v17
	v_cvt_pk_fp8_f32 v15, v18, v19
	v_lshlrev_b32_e32 v20, 16, v21
	v_and_b32_e32 v19, 0xffff0000, v21
	v_mul_f32_e32 v18, 0x41000000, v20
	v_mul_f32_e32 v19, 0x41000000, v19
	v_cvt_pk_fp8_f32 v15, v18, v19 op_sel:[0,0,1]
	v_mov_b32_e32 v52, v17
	v_mov_b32_e32 v53, v17
	v_mov_b32_e32 v54, v17
	v_mov_b32_e32 v55, v17
	v_mov_b64_e32 v[58:59], v[54:55]
	v_mov_b64_e32 v[62:63], v[54:55]
	v_mov_b64_e32 v[66:67], v[54:55]
	v_mov_b64_e32 v[70:71], v[54:55]
	v_mov_b64_e32 v[74:75], v[54:55]
	v_mov_b64_e32 v[78:79], v[54:55]
	v_mov_b64_e32 v[82:83], v[54:55]
	v_mov_b64_e32 v[20:21], v[52:53]
	v_mov_b64_e32 v[24:25], v[52:53]
	v_mov_b64_e32 v[28:29], v[52:53]
	v_mov_b64_e32 v[32:33], v[52:53]
	v_mov_b64_e32 v[36:37], v[52:53]
	v_mov_b64_e32 v[40:41], v[52:53]
	v_mov_b64_e32 v[44:45], v[52:53]
	v_mov_b64_e32 v[48:49], v[52:53]
	v_add_u32_e32 v184, -2, v16
	v_add_u32_e32 v185, -3, v16
	s_add_i32 s68, s55, -16
	v_subrev_u32_e32 v186, 17, v16
	v_subrev_u32_e32 v187, 18, v16
	v_subrev_u32_e32 v188, 19, v16
	s_sub_i32 s69, s55, 32
	v_subrev_u32_e32 v189, 33, v16
	v_subrev_u32_e32 v190, 34, v16
	v_subrev_u32_e32 v191, 35, v16
	s_sub_i32 s70, s55, 48
	v_subrev_u32_e32 v192, 49, v16
	v_subrev_u32_e32 v193, 50, v16
	v_subrev_u32_e32 v194, 51, v16
	v_or_b32_e32 v195, 4, v16
	v_add_u32_e32 v196, 2, v16
	v_add_u32_e32 v197, 1, v16
	s_add_i32 s71, s55, -12
	v_add_u32_e32 v198, -13, v16
	v_add_u32_e32 v199, -14, v16
	v_add_u32_e32 v200, -15, v16
	s_sub_i32 s72, s55, 28
	v_subrev_u32_e32 v201, 29, v16
	v_subrev_u32_e32 v202, 30, v16
	v_subrev_u32_e32 v203, 31, v16
	s_sub_i32 s73, s55, 44
	v_subrev_u32_e32 v204, 45, v16
	v_subrev_u32_e32 v205, 46, v16
	v_subrev_u32_e32 v206, 47, v16
	s_max_i32 s89, s59, 1
	s_mov_b32 s36, 0
	s_add_i32 s37, s84, 64
	v_mov_b32_e32 v224, s37
	ds_read_b64 v[224:225], v224
	v_mov_b32_e32 v19, 0xf149f2ca
	v_mov_b32_e32 v183, 0
	v_mov_b64_e32 v[56:57], v[52:53]
	v_mov_b64_e32 v[60:61], v[52:53]
	v_mov_b64_e32 v[64:65], v[52:53]
	v_mov_b64_e32 v[68:69], v[52:53]
	v_mov_b64_e32 v[72:73], v[52:53]
	v_mov_b64_e32 v[76:77], v[52:53]
	v_mov_b64_e32 v[80:81], v[52:53]
	v_mov_b32_e32 v182, 0
	v_mov_b32_e32 v117, 0xf149f2ca
	v_mov_b32_e32 v216, 0x40a00000
	v_mov_b32_e32 v217, 0xc0a00000
	v_mov_b32_e32 v218, 0xf149f2ca
	v_mov_b32_e32 v219, 0
	v_mov_b32_e32 v220, 0x40a00000
	v_mov_b32_e32 v221, 0xc0a00000
	v_mov_b32_e32 v222, 0xf149f2ca
	v_mov_b32_e32 v223, 0
	v_mov_b64_e32 v[22:23], v[54:55]
	v_mov_b64_e32 v[26:27], v[54:55]
	v_mov_b64_e32 v[30:31], v[54:55]
	v_mov_b64_e32 v[34:35], v[54:55]
	v_mov_b64_e32 v[38:39], v[54:55]
	v_mov_b64_e32 v[42:43], v[54:55]
	v_mov_b64_e32 v[46:47], v[54:55]
	v_mov_b64_e32 v[50:51], v[54:55]
.LBB0_1784:
	s_add_i32 s76, s36, 1
	s_cmp_lt_i32 s76, s59
	s_cselect_b64 s[12:13], -1, 0
	s_cselect_b32 s99, 1, 0
	s_waitcnt vmcnt(0)
	s_waitcnt lgkmcnt(0)
	s_barrier
	s_andn2_b64 vcc, exec, s[12:13]
	s_cbranch_vccnz .LBB0_1796
	v_readfirstlane_b32 s60, v224
	v_readfirstlane_b32 s61, v225
	s_bitcmp1_b32 s76, 0
	s_cselect_b32 s98, 0xe400, 0
	s_add_i32 s98, s85, s98
	s_lshr_b32 s99, s60, 23
	s_and_b32 s99, s99, 6
	s_or_b32 s99, s99, 1
	s_add_i32 s37, s76, 1
	s_cmp_ge_i32 s37, s59
	s_cbranch_scc1 .LBB0_1796
	s_lshl_b32 s37, s37, 6
	s_add_i32 s37, s84, s37
	v_mov_b32_e32 v224, s37
	ds_read_b64 v[224:225], v224

; #define RD16(dst, base, off) asm volatile("ds_read_b128 %0, %1 offset:%2" : "=&v"(dst) : "v"(base), "i"(off) : "memory")
; #define LGKM_W(n) asm volatile("s_waitcnt lgkmcnt(" #n ")" ::: "memory"); SBAR()
; #define QK8_MM(T_) do { i32x8a kf; kf.lo = lo[T_]; kf.hi = hi[T_]; s[T_] = __builtin_amdgcn_mfma_scale_f32_16x16x128_f8f6f4(kf, g.q8, (f32x4){c0, c0, c0, c0}, 0, 0, 0, 0x7f7f7f7f, 0, 0x7c7c7c7c); } while (0)
; #define PV8_RD(dt) do { RD8(f.a[dt][0], vb, (dt) * 16 * VT8ST); RD8(f.a[dt][1], vb, (dt) * 16 * VT8ST + 32); } while (0)
; __device__ __forceinline__ void qk8_tile_c(f32x4 (&s)[4], const GS8& g, const unsigned kb  , const float c0  ) {
;     i32x4a lo[4], hi[4];
;     RD16(lo[0], kb, 0); RD16(hi[0], kb, 16); RD16(lo[1], kb, 16 * K8ST); RD16(hi[1], kb, 16 * K8ST + 16);
;     RD16(lo[2], kb, 32 * K8ST); RD16(hi[2], kb, 32 * K8ST + 16); RD16(lo[3], kb, 48 * K8ST); RD16(hi[3], kb, 48 * K8ST + 16);
;     ...
;     LGKM_W(6); QK8_MM(0); LGKM_W(4); QK8_MM(1); LGKM_W(2); QK8_MM(2); LGKM_W(0); QK8_MM(3);
;     ...
; }
; __device__ __forceinline__ void pv8_issue(VT8Frag& f, const unsigned vb  ) {
;     ...
;     PV8_RD(0); PV8_RD(1); PV8_RD(2); PV8_RD(3); PV8_RD(4); PV8_RD(5); PV8_RD(6); PV8_RD(7);
;     ...
; }
.Lsel_nodma:
	s_lshr_b32 s45, s67, s36
	s_and_b32 s97, s45, 0xff
	s_cbranch_scc0 .LBB0_1798
	ds_read_b128 v[84:87], v208 offset:0
	ds_read_b128 v[88:91], v208 offset:16
	ds_read_b128 v[92:95], v208 offset:0x900
	ds_read_b128 v[96:99], v208 offset:0x910
	ds_read_b128 v[118:121], v208 offset:0x1200
	ds_read_b128 v[122:125], v208 offset:0x1210
	s_and_b32 vcc_lo, s45, 15
	s_cbranch_scc0 .Lsel_g1_pre
	v_and_b32_e32 v18, s45, v154
	v_cmp_eq_u32_e32 vcc, 0, v18
	s_lshr_b32 s44, s66, s36
	s_and_b32 s44, s44, 0xff
	v_cndmask_b32_e32 v210, v216, v181, vcc
	v_mov_b32_e32 v211, v210
	v_mov_b32_e32 v212, v210
	v_mov_b32_e32 v213, v210
	ds_read_b128 v[126:129], v208 offset:0x1b00
	ds_read_b128 v[130:133], v208 offset:0x1b10
	s_waitcnt lgkmcnt(6)
	v_mfma_scale_f32_16x16x128_f8f6f4 v[84:87], v[84:91], v[0:7], v[210:213], v178, v177 op_sel_hi:[0,0,0]
	ds_read_b64 v[148:149], v207 offset:0
	ds_read_b64 v[146:147], v207 offset:32
	ds_read_b64 v[144:145], v207 offset:0x500
	ds_read_b64 v[142:143], v207 offset:0x520
	ds_read_b64 v[140:141], v207 offset:0xa00
	ds_read_b64 v[136:137], v207 offset:0xa20
	ds_read_b64 v[138:139], v207 offset:0xf00
	ds_read_b64 v[134:135], v207 offset:0xf20
	s_waitcnt lgkmcnt(12)
	v_mfma_scale_f32_16x16x128_f8f6f4 v[88:91], v[92:99], v[0:7], v[210:213], v178, v177 op_sel_hi:[0,0,0]
	s_waitcnt lgkmcnt(10)
	v_mfma_scale_f32_16x16x128_f8f6f4 v[92:95], v[118:125], v[0:7], v[210:213], v178, v177 op_sel_hi:[0,0,0]
	s_waitcnt lgkmcnt(8)
	s_cmp_eq_u32 s44, s58
	v_mfma_scale_f32_16x16x128_f8f6f4 v[96:99], v[126:133], v[0:7], v[210:213], v178, v177 op_sel_hi:[0,0,0]
	ds_read_b64 v[132:133], v207 offset:0x1400
	ds_read_b64 v[130:131], v207 offset:0x1420
	ds_read_b64 v[128:129], v207 offset:0x1900
	ds_read_b64 v[126:127], v207 offset:0x1920
	ds_read_b64 v[124:125], v207 offset:0x1e00
	ds_read_b64 v[118:119], v207 offset:0x2300
	s_cbranch_scc1 .Lsel_diag_g0

; __device__ __forceinline__ unsigned pk4_fp8(float a, float b, float c, float d) { unsigned w = 0u; w = __builtin_amdgcn_cvt_pk_fp8_f32(a, b, w, false); w = __builtin_amdgcn_cvt_pk_fp8_f32(c, d, w, true); return w; }
; #define LGKM_W(n) asm volatile("s_waitcnt lgkmcnt(" #n ")" ::: "memory"); SBAR()
; #define PV8_MM(dt) do { g.o[dt] = __builtin_amdgcn_mfma_f32_16x16x32_fp8_fp8(f.a[dt][0], b0, g.o[dt], 0, 0, 0); g.o[dt] = __builtin_amdgcn_mfma_f32_16x16x32_fp8_fp8(f.a[dt][1], b1, g.o[dt], 0, 0, 0); } while (0)
; template <class G> __device__ __forceinline__ void pv8_mm(G& g, const f32x4 (&s)[4], const VT8Frag& f) {
;     ...
;     unsigned pa[4];
; #pragma unroll
;     for (int T_ = 0; T_ < 4; ++T_) pa[T_] = pk4_fp8(s[T_][0], s[T_][1], s[T_][2], s[T_][3]);
;     const long b0 = (long)(((unsigned long long)pa[1] << 32) | pa[0]), b1 = (long)(((unsigned long long)pa[3] << 32) | pa[2]);
;     LGKM_W(14); PV8_MM(0); LGKM_W(12); PV8_MM(1); LGKM_W(10); PV8_MM(2); LGKM_W(8); PV8_MM(3);
;     LGKM_W(6); PV8_MM(4); LGKM_W(4); PV8_MM(5); LGKM_W(2); PV8_MM(6); LGKM_W(0); PV8_MM(7);
;     ...
; }
; template <class G> __device__ __forceinline__ void online_sm8(f32x4 (&s)[4], G& g, const float ref) {
;     ...
;     float ps = 0.f;
; #pragma unroll
;     for (int T_ = 0; T_ < 4; ++T_)
; #pragma unroll
;         for (int i = 0; i < 4; ++i) { s[T_][i] = __builtin_amdgcn_exp2f(s[T_][i]); ps += s[T_][i]; }
;     g.l += ps;
.LBB0_1808:
	v_exp_f32_e32 v240, v84
	v_exp_f32_e32 v241, v85
	ds_read_b64 v[120:121], v207 offset:0x1e20
	ds_read_b64 v[122:123], v207 offset:0x2320
	v_exp_f32_e32 v242, v86
	v_exp_f32_e32 v243, v87
	v_exp_f32_e32 v244, v88
	v_exp_f32_e32 v245, v89
	v_exp_f32_e32 v246, v90
	v_exp_f32_e32 v247, v91
	s_waitcnt lgkmcnt(2)
	v_cvt_pk_fp8_f32 v84, v240, v241
	v_cvt_pk_fp8_f32 v85, v244, v245
	v_cvt_pk_fp8_f32 v84, v242, v243 op_sel:[0,0,1]
	v_cvt_pk_fp8_f32 v85, v246, v247 op_sel:[0,0,1]
	v_exp_f32_e32 v248, v92
	v_exp_f32_e32 v249, v93
	v_mfma_f32_16x16x32_fp8_fp8 v[80:83], v[148:149], v[84:85], v[80:83]
	v_exp_f32_e32 v250, v94
	v_mfma_f32_16x16x32_fp8_fp8 v[76:79], v[144:145], v[84:85], v[76:79]
	v_exp_f32_e32 v251, v95
	v_mfma_f32_16x16x32_fp8_fp8 v[72:75], v[140:141], v[84:85], v[72:75]
	v_exp_f32_e32 v252, v96
	v_mfma_f32_16x16x32_fp8_fp8 v[68:71], v[138:139], v[84:85], v[68:71]
	v_exp_f32_e32 v253, v97
	v_mfma_f32_16x16x32_fp8_fp8 v[64:67], v[132:133], v[84:85], v[64:67]
	v_exp_f32_e32 v254, v98
	v_mfma_f32_16x16x32_fp8_fp8 v[60:63], v[128:129], v[84:85], v[60:63]
	v_exp_f32_e32 v255, v99
	v_mfma_f32_16x16x32_fp8_fp8 v[56:59], v[124:125], v[84:85], v[56:59]
	v_mfma_f32_16x16x32_fp8_fp8 v[52:55], v[118:119], v[84:85], v[52:55]
	s_waitcnt lgkmcnt(0)
	v_cvt_pk_fp8_f32 v86, v248, v249
	v_cvt_pk_fp8_f32 v87, v252, v253
	v_cvt_pk_fp8_f32 v86, v250, v251 op_sel:[0,0,1]
	v_cvt_pk_fp8_f32 v87, v254, v255 op_sel:[0,0,1]
	v_add_f32_e32 v240, v240, v241
	v_add_f32_e32 v242, v242, v243
	v_mfma_f32_16x16x32_fp8_fp8 v[80:83], v[146:147], v[86:87], v[80:83]
	v_add_f32_e32 v244, v244, v245
	v_add_f32_e32 v246, v246, v247
	v_mfma_f32_16x16x32_fp8_fp8 v[76:79], v[142:143], v[86:87], v[76:79]
	v_add_f32_e32 v248, v248, v249
	v_add_f32_e32 v250, v250, v251
	v_mfma_f32_16x16x32_fp8_fp8 v[72:75], v[136:137], v[86:87], v[72:75]
	v_add_f32_e32 v252, v252, v253
	v_add_f32_e32 v254, v254, v255
	v_mfma_f32_16x16x32_fp8_fp8 v[68:71], v[134:135], v[86:87], v[68:71]
	v_add_f32_e32 v240, v240, v242
	v_add_f32_e32 v244, v244, v246
	v_mfma_f32_16x16x32_fp8_fp8 v[64:67], v[130:131], v[86:87], v[64:67]
	v_add_f32_e32 v248, v248, v250
	v_add_f32_e32 v252, v252, v254
	v_mfma_f32_16x16x32_fp8_fp8 v[60:63], v[126:127], v[86:87], v[60:63]
	v_add_f32_e32 v240, v240, v244
	v_add_f32_e32 v248, v248, v252
	v_mfma_f32_16x16x32_fp8_fp8 v[56:59], v[120:121], v[86:87], v[56:59]
	v_add_f32_e32 v240, v240, v248
	v_add_f32_e32 v183, v183, v240
	v_mfma_f32_16x16x32_fp8_fp8 v[52:55], v[122:123], v[86:87], v[52:55]

; #define RD16(dst, base, off) asm volatile("ds_read_b128 %0, %1 offset:%2" : "=&v"(dst) : "v"(base), "i"(off) : "memory")
; #define LGKM_W(n) asm volatile("s_waitcnt lgkmcnt(" #n ")" ::: "memory"); SBAR()
; #define QK8_MM(T_) do { i32x8a kf; kf.lo = lo[T_]; kf.hi = hi[T_]; s[T_] = __builtin_amdgcn_mfma_scale_f32_16x16x128_f8f6f4(kf, g.q8, (f32x4){c0, c0, c0, c0}, 0, 0, 0, 0x7f7f7f7f, 0, 0x7c7c7c7c); } while (0)
; #define PV8_RD(dt) do { RD8(f.a[dt][0], vb, (dt) * 16 * VT8ST); RD8(f.a[dt][1], vb, (dt) * 16 * VT8ST + 32); } while (0)
; __device__ __forceinline__ void qk8_tile_c(f32x4 (&s)[4], const GS8& g, const unsigned kb  , const float c0  ) {
;     i32x4a lo[4], hi[4];
;     RD16(lo[0], kb, 0); RD16(hi[0], kb, 16); RD16(lo[1], kb, 16 * K8ST); RD16(hi[1], kb, 16 * K8ST + 16);
;     RD16(lo[2], kb, 32 * K8ST); RD16(hi[2], kb, 32 * K8ST + 16); RD16(lo[3], kb, 48 * K8ST); RD16(hi[3], kb, 48 * K8ST + 16);
;     ...
;     LGKM_W(6); QK8_MM(0); LGKM_W(4); QK8_MM(1); LGKM_W(2); QK8_MM(2); LGKM_W(0); QK8_MM(3);
;     ...
; }
; __device__ __forceinline__ void pv8_issue(VT8Frag& f, const unsigned vb  ) {
;     ...
;     PV8_RD(0); PV8_RD(1); PV8_RD(2); PV8_RD(3); PV8_RD(4); PV8_RD(5); PV8_RD(6); PV8_RD(7);
;     ...
; }
.Lsel_g1_pre:
	s_lshr_b32 s45, s45, 4
	v_and_b32_e32 v18, s45, v154
	v_cmp_eq_u32_e32 vcc, 0, v18
	s_lshr_b32 s44, s66, s36
	s_and_b32 s44, s44, 0xff
	v_cndmask_b32_e32 v210, v220, v181, vcc
	v_mov_b32_e32 v211, v210
	v_mov_b32_e32 v212, v210
	v_mov_b32_e32 v213, v210
	ds_read_b128 v[126:129], v208 offset:0x1b00
	ds_read_b128 v[130:133], v208 offset:0x1b10
	s_waitcnt lgkmcnt(6)
	v_mfma_scale_f32_16x16x128_f8f6f4 v[84:87], v[84:91], v[8:15], v[210:213], v178, v177 op_sel_hi:[0,0,0]
	ds_read_b64 v[148:149], v207 offset:0
	ds_read_b64 v[146:147], v207 offset:32
	ds_read_b64 v[144:145], v207 offset:0x500
	ds_read_b64 v[142:143], v207 offset:0x520
	ds_read_b64 v[140:141], v207 offset:0xa00
	ds_read_b64 v[136:137], v207 offset:0xa20
	ds_read_b64 v[138:139], v207 offset:0xf00
	ds_read_b64 v[134:135], v207 offset:0xf20
	s_waitcnt lgkmcnt(12)
	v_mfma_scale_f32_16x16x128_f8f6f4 v[88:91], v[92:99], v[8:15], v[210:213], v178, v177 op_sel_hi:[0,0,0]
	s_waitcnt lgkmcnt(10)
	v_mfma_scale_f32_16x16x128_f8f6f4 v[92:95], v[118:125], v[8:15], v[210:213], v178, v177 op_sel_hi:[0,0,0]
	s_waitcnt lgkmcnt(8)
	s_cmp_eq_u32 s44, s58
	v_mfma_scale_f32_16x16x128_f8f6f4 v[96:99], v[126:133], v[8:15], v[210:213], v178, v177 op_sel_hi:[0,0,0]
	ds_read_b64 v[132:133], v207 offset:0x1400
	ds_read_b64 v[130:131], v207 offset:0x1420
	ds_read_b64 v[128:129], v207 offset:0x1900
	ds_read_b64 v[126:127], v207 offset:0x1920
	ds_read_b64 v[124:125], v207 offset:0x1e00
	ds_read_b64 v[118:119], v207 offset:0x2300
	s_cbranch_scc1 .Lsel_diag_g1

; __device__ __forceinline__ unsigned pk4_fp8(float a, float b, float c, float d) { unsigned w = 0u; w = __builtin_amdgcn_cvt_pk_fp8_f32(a, b, w, false); w = __builtin_amdgcn_cvt_pk_fp8_f32(c, d, w, true); return w; }
; #define LGKM_W(n) asm volatile("s_waitcnt lgkmcnt(" #n ")" ::: "memory"); SBAR()
; #define PV8_MM(dt) do { g.o[dt] = __builtin_amdgcn_mfma_f32_16x16x32_fp8_fp8(f.a[dt][0], b0, g.o[dt], 0, 0, 0); g.o[dt] = __builtin_amdgcn_mfma_f32_16x16x32_fp8_fp8(f.a[dt][1], b1, g.o[dt], 0, 0, 0); } while (0)
; template <class G> __device__ __forceinline__ void pv8_mm(G& g, const f32x4 (&s)[4], const VT8Frag& f) {
;     ...
;     unsigned pa[4];
; #pragma unroll
;     for (int T_ = 0; T_ < 4; ++T_) pa[T_] = pk4_fp8(s[T_][0], s[T_][1], s[T_][2], s[T_][3]);
;     const long b0 = (long)(((unsigned long long)pa[1] << 32) | pa[0]), b1 = (long)(((unsigned long long)pa[3] << 32) | pa[2]);
;     LGKM_W(14); PV8_MM(0); LGKM_W(12); PV8_MM(1); LGKM_W(10); PV8_MM(2); LGKM_W(8); PV8_MM(3);
;     LGKM_W(6); PV8_MM(4); LGKM_W(4); PV8_MM(5); LGKM_W(2); PV8_MM(6); LGKM_W(0); PV8_MM(7);
;     ...
; }
; template <class G> __device__ __forceinline__ void online_sm8(f32x4 (&s)[4], G& g, const float ref) {
;     ...
;     float ps = 0.f;
; #pragma unroll
;     for (int T_ = 0; T_ < 4; ++T_)
; #pragma unroll
;         for (int i = 0; i < 4; ++i) { s[T_][i] = __builtin_amdgcn_exp2f(s[T_][i]); ps += s[T_][i]; }
;     g.l += ps;
.LBB0_1797:
	v_exp_f32_e32 v240, v84
	v_exp_f32_e32 v241, v85
	ds_read_b64 v[120:121], v207 offset:0x1e20
	ds_read_b64 v[122:123], v207 offset:0x2320
	v_exp_f32_e32 v242, v86
	v_exp_f32_e32 v243, v87
	v_exp_f32_e32 v244, v88
	v_exp_f32_e32 v245, v89
	v_exp_f32_e32 v246, v90
	v_exp_f32_e32 v247, v91
	s_waitcnt lgkmcnt(2)
	v_cvt_pk_fp8_f32 v84, v240, v241
	v_cvt_pk_fp8_f32 v85, v244, v245
	v_cvt_pk_fp8_f32 v84, v242, v243 op_sel:[0,0,1]
	v_cvt_pk_fp8_f32 v85, v246, v247 op_sel:[0,0,1]
	v_exp_f32_e32 v248, v92
	v_exp_f32_e32 v249, v93
	v_mfma_f32_16x16x32_fp8_fp8 v[48:51], v[148:149], v[84:85], v[48:51]
	v_exp_f32_e32 v250, v94
	v_mfma_f32_16x16x32_fp8_fp8 v[44:47], v[144:145], v[84:85], v[44:47]
	v_exp_f32_e32 v251, v95
	v_mfma_f32_16x16x32_fp8_fp8 v[40:43], v[140:141], v[84:85], v[40:43]
	v_exp_f32_e32 v252, v96
	v_mfma_f32_16x16x32_fp8_fp8 v[36:39], v[138:139], v[84:85], v[36:39]
	v_exp_f32_e32 v253, v97
	v_mfma_f32_16x16x32_fp8_fp8 v[32:35], v[132:133], v[84:85], v[32:35]
	v_exp_f32_e32 v254, v98
	v_mfma_f32_16x16x32_fp8_fp8 v[28:31], v[128:129], v[84:85], v[28:31]
	v_exp_f32_e32 v255, v99
	v_mfma_f32_16x16x32_fp8_fp8 v[24:27], v[124:125], v[84:85], v[24:27]
	v_mfma_f32_16x16x32_fp8_fp8 v[20:23], v[118:119], v[84:85], v[20:23]
	s_waitcnt lgkmcnt(0)
	v_cvt_pk_fp8_f32 v86, v248, v249
	v_cvt_pk_fp8_f32 v87, v252, v253
	v_cvt_pk_fp8_f32 v86, v250, v251 op_sel:[0,0,1]
	v_cvt_pk_fp8_f32 v87, v254, v255 op_sel:[0,0,1]
	v_add_f32_e32 v240, v240, v241
	v_add_f32_e32 v242, v242, v243
	v_mfma_f32_16x16x32_fp8_fp8 v[48:51], v[146:147], v[86:87], v[48:51]
	v_add_f32_e32 v244, v244, v245
	v_add_f32_e32 v246, v246, v247
	v_mfma_f32_16x16x32_fp8_fp8 v[44:47], v[142:143], v[86:87], v[44:47]
	v_add_f32_e32 v248, v248, v249
	v_add_f32_e32 v250, v250, v251
	v_mfma_f32_16x16x32_fp8_fp8 v[40:43], v[136:137], v[86:87], v[40:43]
	v_add_f32_e32 v252, v252, v253
	v_add_f32_e32 v254, v254, v255
	v_mfma_f32_16x16x32_fp8_fp8 v[36:39], v[134:135], v[86:87], v[36:39]
	v_add_f32_e32 v240, v240, v242
	v_add_f32_e32 v244, v244, v246
	v_mfma_f32_16x16x32_fp8_fp8 v[32:35], v[130:131], v[86:87], v[32:35]
	v_add_f32_e32 v248, v248, v250
	v_add_f32_e32 v252, v252, v254
	v_mfma_f32_16x16x32_fp8_fp8 v[28:31], v[126:127], v[86:87], v[28:31]
	v_add_f32_e32 v240, v240, v244
	v_add_f32_e32 v248, v248, v252
	v_mfma_f32_16x16x32_fp8_fp8 v[24:27], v[120:121], v[86:87], v[24:27]
	v_add_f32_e32 v240, v240, v248
	v_add_f32_e32 v182, v182, v240
	v_mfma_f32_16x16x32_fp8_fp8 v[20:23], v[122:123], v[86:87], v[20:23]
	s_branch .LBB0_1798
